# P0 row pass: both half-row load pairs issued together (one memory round trip per row instead of two)
# baseline (speedup 1.0000x reference)
; __device__ __forceinline__ unsigned pk2(float lo, float hi) { return f2bf(lo) | (f2bf(hi) << 16); }
; __device__ __forceinline__ void p0_rows(const float* xin, bf16* XB, float* RS, int gw, int NGW, int lane) {
;     for (int m = gw; m < M; m += NGW) {
;         float ss = 0.f;
; #pragma unroll
;         for (int j = 0; j < 2; ++j) { const float* p = xin + (size_t)m * D + 512 * j + 8 * lane; const f32x4 a = __builtin_nontemporal_load((const f32x4*)p), b = __builtin_nontemporal_load((const f32x4*)(p + 4));
;             ss += (a.x * a.x + a.y * a.y) + (a.z * a.z + a.w * a.w) + (b.x * b.x + b.y * b.y) + (b.z * b.z + b.w * b.w);
;             v4u w; w.x = pk2(a.x, a.y); w.y = pk2(a.z, a.w); w.z = pk2(b.x, b.y); w.w = pk2(b.z, b.w); *(v4u*)(XB + (size_t)m * D + 512 * j + 8 * lane) = w; }
;         ss = wave_sum(ss);
;         if (lane == 0) *(f32x4*)(RS + 4 * (size_t)m) = (f32x4){ss, 0.f, 0.f, 0.f};
;     }
.LBB0_794:
	global_load_dwordx4 v[8:11], v[6:7], off nt
	global_load_dwordx4 v[12:15], v[6:7], off offset:16 nt
	global_load_dwordx4 v[24:27], v[6:7], off offset:2048 nt
	global_load_dwordx4 v[28:31], v[6:7], off offset:2064 nt
	s_waitcnt vmcnt(2)
	v_and_b32_sdwa v2, v11, v235 dst_sel:DWORD dst_unused:UNUSED_PAD src0_sel:WORD_1 src1_sel:DWORD
	v_and_b32_sdwa v16, v9, v235 dst_sel:DWORD dst_unused:UNUSED_PAD src0_sel:WORD_1 src1_sel:DWORD
	v_and_b32_sdwa v17, v14, v235 dst_sel:DWORD dst_unused:UNUSED_PAD src0_sel:WORD_1 src1_sel:DWORD
	v_and_b32_sdwa v19, v15, v235 dst_sel:DWORD dst_unused:UNUSED_PAD src0_sel:WORD_1 src1_sel:DWORD
	v_and_b32_sdwa v20, v13, v235 dst_sel:DWORD dst_unused:UNUSED_PAD src0_sel:WORD_1 src1_sel:DWORD
	v_and_b32_sdwa v0, v10, v235 dst_sel:DWORD dst_unused:UNUSED_PAD src0_sel:WORD_1 src1_sel:DWORD
	v_and_b32_sdwa v1, v8, v235 dst_sel:DWORD dst_unused:UNUSED_PAD src0_sel:WORD_1 src1_sel:DWORD
	v_and_b32_sdwa v18, v12, v235 dst_sel:DWORD dst_unused:UNUSED_PAD src0_sel:WORD_1 src1_sel:DWORD
	v_add3_u32 v2, v11, v2, s69
	v_add3_u32 v16, v9, v16, s69
	v_add3_u32 v21, v14, v17, s69
	v_add3_u32 v17, v15, v19, s69
	v_add3_u32 v19, v13, v20, s69
	v_add3_u32 v1, v8, v1, s69
	v_add3_u32 v0, v10, v0, s69
	v_add3_u32 v18, v12, v18, s69
	v_and_b32_e32 v2, 0xffff0000, v2
	v_and_b32_e32 v16, 0xffff0000, v16
	v_and_b32_e32 v20, 0xffff0000, v17
	v_and_b32_e32 v22, 0xffff0000, v19
	v_or_b32_sdwa v17, v2, v0 dst_sel:DWORD dst_unused:UNUSED_PAD src0_sel:DWORD src1_sel:WORD_1
	v_or_b32_sdwa v16, v16, v1 dst_sel:DWORD dst_unused:UNUSED_PAD src0_sel:DWORD src1_sel:WORD_1
	v_or_b32_sdwa v19, v20, v21 dst_sel:DWORD dst_unused:UNUSED_PAD src0_sel:DWORD src1_sel:WORD_1
	v_or_b32_sdwa v18, v22, v18 dst_sel:DWORD dst_unused:UNUSED_PAD src0_sel:DWORD src1_sel:WORD_1
	global_store_dwordx4 v[4:5], v[16:19], off offset:-1024
	v_mul_f32_e32 v0, v9, v9
	v_mul_f32_e32 v1, v11, v11
	v_mul_f32_e32 v2, v13, v13
	v_fmac_f32_e32 v0, v8, v8
	v_fmac_f32_e32 v1, v10, v10
	v_fmac_f32_e32 v2, v12, v12
	v_add_f32_e32 v0, v0, v1
	v_mul_f32_e32 v9, v15, v15
	v_add_f32_e32 v0, v0, v2
	v_fmac_f32_e32 v9, v14, v14
	v_add_f32_e32 v0, v9, v0
	s_waitcnt vmcnt(2)
	v_mul_f32_e32 v1, v25, v25
	v_mul_f32_e32 v2, v27, v27
	s_waitcnt vmcnt(1)
	v_mul_f32_e32 v8, v29, v29
	v_fmac_f32_e32 v1, v24, v24
	v_fmac_f32_e32 v2, v26, v26
	v_mul_f32_e32 v9, v31, v31
	v_fmac_f32_e32 v8, v28, v28
	v_add_f32_e32 v1, v1, v2
	v_fmac_f32_e32 v9, v30, v30
	v_add_f32_e32 v1, v1, v8
	v_add_f32_e32 v1, v9, v1
	v_add_f32_e32 v0, v0, v1
	ds_swizzle_b32 v1, v0 offset:swizzle(SWAP,1)
	v_and_b32_sdwa v12, v27, v235 dst_sel:DWORD dst_unused:UNUSED_PAD src0_sel:WORD_1 src1_sel:DWORD
	v_and_b32_sdwa v13, v25, v235 dst_sel:DWORD dst_unused:UNUSED_PAD src0_sel:WORD_1 src1_sel:DWORD
	v_and_b32_sdwa v8, v31, v235 dst_sel:DWORD dst_unused:UNUSED_PAD src0_sel:WORD_1 src1_sel:DWORD
	v_and_b32_sdwa v9, v29, v235 dst_sel:DWORD dst_unused:UNUSED_PAD src0_sel:WORD_1 src1_sel:DWORD
	s_waitcnt lgkmcnt(0)
	v_add_f32_e32 v0, v0, v1
	ds_swizzle_b32 v1, v0 offset:swizzle(SWAP,2)
	v_and_b32_sdwa v10, v26, v235 dst_sel:DWORD dst_unused:UNUSED_PAD src0_sel:WORD_1 src1_sel:DWORD
	v_and_b32_sdwa v11, v24, v235 dst_sel:DWORD dst_unused:UNUSED_PAD src0_sel:WORD_1 src1_sel:DWORD
	v_and_b32_sdwa v14, v30, v235 dst_sel:DWORD dst_unused:UNUSED_PAD src0_sel:WORD_1 src1_sel:DWORD
	v_and_b32_sdwa v2, v28, v235 dst_sel:DWORD dst_unused:UNUSED_PAD src0_sel:WORD_1 src1_sel:DWORD
	s_waitcnt lgkmcnt(0)
	v_add_f32_e32 v0, v0, v1
	ds_swizzle_b32 v1, v0 offset:swizzle(SWAP,4)
	v_add3_u32 v12, v27, v12, s69
	v_add3_u32 v13, v25, v13, s69
	v_add3_u32 v8, v31, v8, s69
	v_add3_u32 v9, v29, v9, s69
	s_waitcnt lgkmcnt(0)
	v_add_f32_e32 v0, v0, v1
	ds_swizzle_b32 v1, v0 offset:swizzle(SWAP,8)
	v_add3_u32 v11, v24, v11, s69
	v_add3_u32 v10, v26, v10, s69
	v_add3_u32 v2, v28, v2, s69
	v_add3_u32 v14, v30, v14, s69
	s_waitcnt lgkmcnt(0)
	v_add_f32_e32 v0, v0, v1
	ds_swizzle_b32 v1, v0 offset:swizzle(SWAP,16)
	v_and_b32_e32 v12, 0xffff0000, v12
	v_and_b32_e32 v13, 0xffff0000, v13
	v_and_b32_e32 v15, 0xffff0000, v8
	v_and_b32_e32 v24, 0xffff0000, v9
	s_waitcnt lgkmcnt(0)
	v_add_f32_e32 v0, v0, v1
	v_or_b32_sdwa v9, v12, v10 dst_sel:DWORD dst_unused:UNUSED_PAD src0_sel:DWORD src1_sel:WORD_1
	v_or_b32_sdwa v8, v13, v11 dst_sel:DWORD dst_unused:UNUSED_PAD src0_sel:DWORD src1_sel:WORD_1
	v_or_b32_sdwa v11, v15, v14 dst_sel:DWORD dst_unused:UNUSED_PAD src0_sel:DWORD src1_sel:WORD_1
	v_or_b32_sdwa v10, v24, v2 dst_sel:DWORD dst_unused:UNUSED_PAD src0_sel:DWORD src1_sel:WORD_1
	v_readlane_b32 s11, v0, 0
	v_readlane_b32 s12, v0, 32
	global_store_dwordx4 v[4:5], v[8:11], off
	s_and_saveexec_b64 s[8:9], vcc
	s_cbranch_execz .LBB0_793
	v_mov_b32_e32 v0, s12
	v_add_f32_e32 v0, s11, v0
	v_mov_b32_e32 v1, v3
	v_mov_b32_e32 v2, v3
	global_store_dwordx4 v3, v[0:3], s[0:1]
	s_branch .LBB0_793
